# moe2 GEMM: block-scaled fp8 MFMAs (scales 2^-5 and 1.0) issued as plain v_mfma_f32_16x16x128_f8f6f4, the exact 2^-5 factor folded into the epilogue's first accumulator use (pk_add -> pk_fma, bit-ident
# baseline (speedup 1.0000x reference)
; #define LAS __attribute__((address_space(3)))
; __device__ __forceinline__ int opaque_tid(int wave) { int l; asm volatile("v_mbcnt_lo_u32_b32 %0, -1, 0\n\tv_mbcnt_hi_u32_b32 %0, -1, %0" : "=v"(l)); return wave * 64 + l; }
; __global__ void __launch_bounds__(NWAVES * 64, 2) fwd_kernel(Args args) {
;     extern __shared__ __attribute__((aligned(16))) unsigned char lds[];
;     Frame F;
;     F.lds = (LAS unsigned char*)lds; F.ldsg = (char*)lds;
;     F.wave0 = __builtin_amdgcn_readfirstlane((int)(threadIdx.x >> 6));
;     F.tid = opaque_tid(F.wave0); F.lane = F.tid & 63; F.wave = F.wave0;
;     F.G = gridDim.x; F.bid = blockIdx.x; F.gw = blockIdx.x * NWAVES + F.wave; F.NGW = F.G * NWAVES;
;     F.out = args.out; F.ws = args.ws; F.ctl = (gu32*)(args.ws + WS_CTL);
;     volatile LAS unsigned* MISC = (volatile LAS unsigned*)(F.lds + MISC_OFF);
;     for (int u = F.tid; u < (LDS_BYTES - MISC_OFF) / 4; u += NWAVES * 64) MISC[u] = 0u;
;     __syncthreads();
_Z10fwd_kernel4Args:
	s_mov_b32 s100, 0x3d000000
	s_mov_b32 s101, 0x3d000000
	s_mov_b64 s[88:89], s[0:1]
	s_load_dword s90, s[0:1], 0xe8
	v_readfirstlane_b32 s0, v0
	s_lshr_b32 s53, s0, 6
	s_andn2_b32 s0, s0, 63
	v_mbcnt_lo_u32_b32 v26, -1, 0
	v_mbcnt_hi_u32_b32 v26, -1, v26
	v_writelane_b32 v232, s0, 0
	v_add_u32_e32 v0, s0, v26
	s_add_u32 s0, s88, 0xe8
	s_addc_u32 s1, s89, 0
	v_writelane_b32 v232, s0, 1
	s_mov_b32 s73, s2
	s_nop 0
	v_writelane_b32 v232, s1, 2
	s_movk_i32 s0, 0x1000
	v_cmp_gt_i32_e32 vcc, s0, v0
	s_and_saveexec_b64 s[0:1], vcc
	s_cbranch_execz .LBB0_3
	s_lshl_b32 s2, s53, 8
	s_add_i32 s2, s2, 0
	v_lshl_add_u32 v2, v26, 2, s2
	v_add_u32_e32 v1, 0xfffffe00, v0
	v_add_u32_e32 v2, 0x20000, v2
	s_mov_b64 s[2:3], 0
	v_mov_b32_e32 v3, 0
	s_movk_i32 s4, 0xdff

; #define PG8_STAGE(bufoff, gbase, v0, v1) do { glds16_s((gbase), (v0), ldsbase + (unsigned)(bufoff)); glds16_s((gbase), (v1), ldsbase + (unsigned)(bufoff) + 8192u); } while (0)
; #define PG8_LDA(dst, b, h) do { _Pragma("unroll") for (int m = 0; m < 4; ++m) _Pragma("unroll") for (int k = 0; k < 2; ++k) dst[m][k] = *(const LAS bf16x8*)(lds + PG8_SA(b, h) + aoff + m * 2048 + k * 1024); } while (0)
; #define PG8_LDB(dst, b, h) do { _Pragma("unroll") for (int n = 0; n < 2; ++n) _Pragma("unroll") for (int k = 0; k < 2; ++k) dst[n][k] = *(const LAS bf16x8*)(lds + PG8_SB(b, h) + boff + n * 2048 + k * 1024); } while (0)
; #define PG8_WAIT_V(n) asm volatile("s_waitcnt vmcnt(" #n ")" ::: "memory")
; #define PG8_WAIT_L(n) asm volatile("s_waitcnt lgkmcnt(" #n ")" ::: "memory")
; #define PG8_BAR __builtin_amdgcn_s_barrier()
; #define PG8_SCHED __builtin_amdgcn_sched_barrier(0)
; template <class Epi, class Sched, bool ALIGN_EPI, bool FP8 = false>
; __device__ __forceinline__ void gemm_phase(LAS unsigned char* lds, const bf16_t* A, const bf16_t* Bt, const int K, const Sched& S, const Epi& E, const int wave_in) {
;     ...
;             PG8_LDB(B0, 0, 0); PG8_LDB(B1, 0, 1); PG8_SCHED; PG8_LDA(At, 0, 0); PG8_STAGE(PG8_SA(1, 1), a1, vA[1][0], vA[1][1]);
;             PG8_WAIT_V(8); PG8_WAIT_L(0); PG8_BAR; PG8_MMA(0, 0, At, B0); PG8_MMA(0, 1, At, B1); PG8_BAR; PG8_SCHED;
;             PG8_LDA(At, 0, 1); PG8_STAGE(PG8_SB(0, 0), b2, voffB[0], voffB[1]); PG8_STAGE(PG8_SB(0, 1), b2 + hstep, voffB[0], voffB[1]); PG8_STAGE(PG8_SA(0, 0), a2, w00, w01);
;             PG8_WAIT_V(8); PG8_WAIT_L(0); PG8_BAR; PG8_MMA(1, 0, At, B0); PG8_MMA(1, 1, At, B1); PG8_BAR; PG8_SCHED;
;             PG8_LDB(B0, 1, 0); PG8_LDB(B1, 1, 1); PG8_SCHED; PG8_LDA(At, 1, 0); PG8_STAGE(PG8_SA(0, 1), a2, w10, w11);
;             PG8_WAIT_V(8); PG8_WAIT_L(0); PG8_BAR; PG8_MMA(0, 0, At, B0); PG8_MMA(0, 1, At, B1); PG8_BAR; PG8_SCHED;
.LBB0_1139:
	s_add_u32 s60, s14, 0x100
	s_addc_u32 s61, s15, 0
	v_add_u32_e32 v2, 0x10000, v169
	v_add_u32_e32 v6, 0x14000, v169
	s_cmp_eq_u32 s89, 4
	ds_read_b128 v[26:29], v2
	ds_read_b128 v[30:33], v2 offset:1024
	ds_read_b128 v[18:21], v2 offset:2048
	ds_read_b128 v[22:25], v2 offset:3072
	ds_read_b128 v[10:13], v6
	ds_read_b128 v[14:17], v6 offset:1024
	ds_read_b128 v[2:5], v6 offset:2048
	ds_read_b128 v[6:9], v6 offset:3072
	s_cselect_b64 vcc, -1, 0
	s_and_b64 s[10:11], vcc, exec
	s_cselect_b32 s92, s76, s60
	s_cselect_b32 s93, s77, s61
	s_cselect_b32 s16, s4, s0
	s_cselect_b32 s17, s5, s1
	s_add_u32 s10, s92, 0x80
	s_addc_u32 s11, s93, 0
	s_add_u32 s12, s14, 0x80
	v_cndmask_b32_e32 v179, v175, v171, vcc
	v_cndmask_b32_e32 v181, v178, v173, vcc
	s_addc_u32 s13, s15, 0
	v_cndmask_b32_e32 v180, v176, v172, vcc
	ds_read_b128 v[198:201], v170
	ds_read_b128 v[202:205], v170 offset:1024
	ds_read_b128 v[206:209], v170 offset:2048
	ds_read_b128 v[210:213], v170 offset:3072
	ds_read_b128 v[214:217], v170 offset:4096
	ds_read_b128 v[218:221], v170 offset:5120
	ds_read_b128 v[222:225], v170 offset:6144
	ds_read_b128 v[226:229], v170 offset:7168
	s_mov_b32 m0, s65
	s_nop 0
	global_load_lds_dwordx4 v178, s[12:13]
	s_add_u32 s14, s16, 0x80
	s_mov_b32 m0, s66
	s_nop 0
	global_load_lds_dwordx4 v177, s[12:13]
	s_waitcnt vmcnt(8)
	s_waitcnt lgkmcnt(0)
	s_addc_u32 s15, s17, 0
	s_barrier
	s_setprio 1
	s_waitcnt lgkmcnt(6)
	v_mfma_f32_16x16x128_f8f6f4 v[160:163], v[26:33], v[198:205], v[160:163]
	v_mfma_f32_16x16x128_f8f6f4 v[156:159], v[18:25], v[198:205], v[156:159]
	s_waitcnt lgkmcnt(4)
	v_mfma_f32_16x16x128_f8f6f4 v[142:145], v[26:33], v[206:213], v[142:145]
	v_mfma_f32_16x16x128_f8f6f4 v[138:141], v[18:25], v[206:213], v[138:141]
	s_waitcnt lgkmcnt(2)
	v_mfma_f32_16x16x128_f8f6f4 v[126:129], v[26:33], v[214:221], v[126:129]
	v_mfma_f32_16x16x128_f8f6f4 v[122:125], v[18:25], v[214:221], v[122:125]
	s_waitcnt lgkmcnt(0)
	v_mfma_f32_16x16x128_f8f6f4 v[110:113], v[26:33], v[222:229], v[110:113]
	v_mfma_f32_16x16x128_f8f6f4 v[106:109], v[18:25], v[222:229], v[106:109]
	s_setprio 0
	s_setprio 1
	v_mfma_f32_16x16x128_f8f6f4 v[152:155], v[10:17], v[198:205], v[152:155]
	v_mfma_f32_16x16x128_f8f6f4 v[148:151], v[2:9], v[198:205], v[148:151]
	v_mfma_f32_16x16x128_f8f6f4 v[134:137], v[10:17], v[206:213], v[134:137]
	v_mfma_f32_16x16x128_f8f6f4 v[130:133], v[2:9], v[206:213], v[130:133]
	v_mfma_f32_16x16x128_f8f6f4 v[118:121], v[10:17], v[214:221], v[118:121]
	v_mfma_f32_16x16x128_f8f6f4 v[114:117], v[2:9], v[214:221], v[114:117]
	v_mfma_f32_16x16x128_f8f6f4 v[102:105], v[10:17], v[222:229], v[102:105]
	v_mfma_f32_16x16x128_f8f6f4 v[98:101], v[2:9], v[222:229], v[98:101]
	s_setprio 0
	s_barrier
	ds_read_b128 v[198:201], v170 offset:16384
	ds_read_b128 v[202:205], v170 offset:17408
	ds_read_b128 v[206:209], v170 offset:18432
	ds_read_b128 v[210:213], v170 offset:19456
	ds_read_b128 v[214:217], v170 offset:20480
	ds_read_b128 v[218:221], v170 offset:21504
	ds_read_b128 v[222:225], v170 offset:22528
	ds_read_b128 v[226:229], v170 offset:23552
	s_mov_b32 m0, s27
	s_nop 0
	global_load_lds_dwordx4 v0, s[16:17]
	s_nop 0
	s_mov_b32 m0, s48
	s_nop 0
	global_load_lds_dwordx4 v147, s[16:17]
	s_add_u32 s12, s16, 0x20000
	s_addc_u32 s13, s17, 0
	s_mov_b32 m0, s49
	s_nop 0
	global_load_lds_dwordx4 v0, s[12:13]
	s_nop 0
	s_mov_b32 m0, s50
	s_nop 0
	global_load_lds_dwordx4 v147, s[12:13]
	s_mov_b32 m0, s39
	s_nop 0
	global_load_lds_dwordx4 v179, s[92:93]
	s_nop 0
	s_mov_b32 m0, s51
	s_nop 0
	global_load_lds_dwordx4 v180, s[92:93]
	s_waitcnt vmcnt(8)
	s_waitcnt lgkmcnt(0)
	s_barrier
	s_setprio 1
	s_waitcnt lgkmcnt(6)
	v_mfma_f32_16x16x128_f8f6f4 v[94:97], v[26:33], v[198:205], v[94:97]
	v_mfma_f32_16x16x128_f8f6f4 v[90:93], v[18:25], v[198:205], v[90:93]
	s_waitcnt lgkmcnt(4)
	v_mfma_f32_16x16x128_f8f6f4 v[78:81], v[26:33], v[206:213], v[78:81]
	v_mfma_f32_16x16x128_f8f6f4 v[74:77], v[18:25], v[206:213], v[74:77]
	s_waitcnt lgkmcnt(2)
	v_mfma_f32_16x16x128_f8f6f4 v[62:65], v[26:33], v[214:221], v[62:65]
	v_mfma_f32_16x16x128_f8f6f4 v[58:61], v[18:25], v[214:221], v[58:61]
	s_waitcnt lgkmcnt(0)
	v_mfma_f32_16x16x128_f8f6f4 v[46:49], v[26:33], v[222:229], v[46:49]
	v_mfma_f32_16x16x128_f8f6f4 v[42:45], v[18:25], v[222:229], v[42:45]
	s_setprio 0
	s_setprio 1
	v_mfma_f32_16x16x128_f8f6f4 v[86:89], v[10:17], v[198:205], v[86:89]
	v_mfma_f32_16x16x128_f8f6f4 v[82:85], v[2:9], v[198:205], v[82:85]
	v_mfma_f32_16x16x128_f8f6f4 v[70:73], v[10:17], v[206:213], v[70:73]
	v_mfma_f32_16x16x128_f8f6f4 v[66:69], v[2:9], v[206:213], v[66:69]
	v_mfma_f32_16x16x128_f8f6f4 v[54:57], v[10:17], v[214:221], v[54:57]
	v_mfma_f32_16x16x128_f8f6f4 v[50:53], v[2:9], v[214:221], v[50:53]
	v_mfma_f32_16x16x128_f8f6f4 v[38:41], v[10:17], v[222:229], v[38:41]
	v_mfma_f32_16x16x128_f8f6f4 v[34:37], v[2:9], v[222:229], v[34:37]
	s_setprio 0
	s_barrier
	v_add_u32_e32 v14, 0x18000, v169
	v_add_u32_e32 v30, 0x1c000, v169
	ds_read_b128 v[2:5], v14
	ds_read_b128 v[6:9], v14 offset:1024
	ds_read_b128 v[10:13], v14 offset:2048
	ds_read_b128 v[14:17], v14 offset:3072
	ds_read_b128 v[18:21], v30
	ds_read_b128 v[22:25], v30 offset:1024
	ds_read_b128 v[26:29], v30 offset:2048
	ds_read_b128 v[30:33], v30 offset:3072
	ds_read_b128 v[198:201], v170 offset:32768
	ds_read_b128 v[202:205], v170 offset:33792
	ds_read_b128 v[206:209], v170 offset:34816
	ds_read_b128 v[210:213], v170 offset:35840
	ds_read_b128 v[214:217], v170 offset:36864
	ds_read_b128 v[218:221], v170 offset:37888
	ds_read_b128 v[222:225], v170 offset:38912
	ds_read_b128 v[226:229], v170 offset:39936
	s_mov_b32 m0, s52
	s_nop 0
	global_load_lds_dwordx4 v181, s[92:93]
	v_cndmask_b32_e32 v197, v177, v174, vcc
	s_mov_b32 m0, s53
	s_nop 0
	global_load_lds_dwordx4 v197, s[92:93]
	s_waitcnt vmcnt(8)
	s_waitcnt lgkmcnt(0)
	s_barrier
; #define LAS __attribute__((address_space(3)))
; __device__ __forceinline__ unsigned cvt_fp8x4(float a, float b, float c, float d) { int w = __builtin_amdgcn_cvt_pk_fp8_f32(a, b, 0, false); w = __builtin_amdgcn_cvt_pk_fp8_f32(c, d, w, true); return (unsigned)w; }
; #define PG8_STAGE(bufoff, gbase, v0, v1) do { glds16_s((gbase), (v0), ldsbase + (unsigned)(bufoff)); glds16_s((gbase), (v1), ldsbase + (unsigned)(bufoff) + 8192u); } while (0)
; #define PG8_LDA(dst, b, h) do { _Pragma("unroll") for (int m = 0; m < 4; ++m) _Pragma("unroll") for (int k = 0; k < 2; ++k) dst[m][k] = *(const LAS bf16x8*)(lds + PG8_SA(b, h) + aoff + m * 2048 + k * 1024); } while (0)
; #define PG8_BAR __builtin_amdgcn_s_barrier()
;     __device__ __forceinline__ void operator()(const f32x4 (&acc)[2][2][4][2], const Unit& u, int wr, int wc, int fr, int fq, const LAS unsigned char* epl) const {
;     ...
;             for (int m = 0; m < 4; ++m) { const int sl = ai * HALF + wr * 64 + m * 16 + fr;
;                 const float gate = *(const LAS float*)(epl + 2048 + sl * 4);
;                 unsigned char* rowp = (unsigned char*)YK + (size_t)(u.pm * BM + sl) * DM + col0;
;                 const float g8 = gate * YK8_SCALE;
; #pragma unroll
;                 for (int bj = 0; bj < 2; ++bj) { const f32x4 a0 = (acc[ai][bj][m][0] + bv[bj][0]) * g8, a1 = (acc[ai][bj][m][1] + bv[bj][1]) * g8;
;                     u32x2 w8; w8.x = cvt_fp8x4(a0[0], a0[1], a0[2], a0[3]); w8.y = cvt_fp8x4(a1[0], a1[1], a1[2], a1[3]); *(u32x2*)(rowp + bj * HALF) = w8; } }
; template <class Epi, class Sched, bool ALIGN_EPI, bool FP8 = false>
; __device__ __forceinline__ void gemm_phase(LAS unsigned char* lds, const bf16_t* A, const bf16_t* Bt, const int K, const Sched& S, const Epi& E, const int wave_in) {
;     ...
;             PG8_LDA(At, 1, 1); PG8_STAGE(PG8_SB(1, 0), b3, voffB[0], voffB[1]); PG8_STAGE(PG8_SB(1, 1), b3 + hstep, voffB[0], voffB[1]); PG8_STAGE(PG8_SA(1, 0), a3, w00, w01);
;             PG8_WAIT_V(8); PG8_WAIT_L(0); PG8_BAR; PG8_MMA(1, 0, At, B0); PG8_MMA(1, 1, At, B1); PG8_BAR; PG8_SCHED;
;         }
;         if constexpr (FP8) asm volatile("s_nop 15\n\ts_nop 15" ::: "memory");
;         if constexpr (ALIGN_EPI) { if (wr == 0) PG8_BAR; }
;         { int fr_ = fr, fq_ = fq; asm volatile("" : "+v"(fr_), "+v"(fq_)); E(acc, cur, wr, wc, fr_, fq_, lds + EPI_LDS_OFF + (ui & 1) * EPI_LDS_BUF); }
	s_setprio 1
	s_waitcnt lgkmcnt(6)
	v_mfma_f32_16x16x128_f8f6f4 v[160:163], v[2:9], v[198:205], v[160:163]
	v_mfma_f32_16x16x128_f8f6f4 v[156:159], v[10:17], v[198:205], v[156:159]
	s_waitcnt lgkmcnt(4)
	v_mfma_f32_16x16x128_f8f6f4 v[142:145], v[2:9], v[206:213], v[142:145]
	v_mfma_f32_16x16x128_f8f6f4 v[138:141], v[10:17], v[206:213], v[138:141]
	s_waitcnt lgkmcnt(2)
	v_mfma_f32_16x16x128_f8f6f4 v[126:129], v[2:9], v[214:221], v[126:129]
	v_mfma_f32_16x16x128_f8f6f4 v[122:125], v[10:17], v[214:221], v[122:125]
	s_waitcnt lgkmcnt(0)
	v_mfma_f32_16x16x128_f8f6f4 v[110:113], v[2:9], v[222:229], v[110:113]
	v_mfma_f32_16x16x128_f8f6f4 v[106:109], v[10:17], v[222:229], v[106:109]
	s_setprio 0
	s_setprio 1
	v_mfma_f32_16x16x128_f8f6f4 v[152:155], v[18:25], v[198:205], v[152:155]
	v_mfma_f32_16x16x128_f8f6f4 v[148:151], v[26:33], v[198:205], v[148:151]
	v_mfma_f32_16x16x128_f8f6f4 v[134:137], v[18:25], v[206:213], v[134:137]
	v_mfma_f32_16x16x128_f8f6f4 v[130:133], v[26:33], v[206:213], v[130:133]
	v_mfma_f32_16x16x128_f8f6f4 v[118:121], v[18:25], v[214:221], v[118:121]
	v_mfma_f32_16x16x128_f8f6f4 v[114:117], v[26:33], v[214:221], v[114:117]
	v_mfma_f32_16x16x128_f8f6f4 v[102:105], v[18:25], v[222:229], v[102:105]
	v_mfma_f32_16x16x128_f8f6f4 v[98:101], v[26:33], v[222:229], v[98:101]
	s_setprio 0
	s_barrier
	ds_read_b128 v[198:201], v170 offset:49152
	ds_read_b128 v[202:205], v170 offset:50176
	ds_read_b128 v[206:209], v170 offset:51200
	ds_read_b128 v[210:213], v170 offset:52224
	ds_read_b128 v[214:217], v170 offset:53248
	ds_read_b128 v[218:221], v170 offset:54272
	ds_read_b128 v[222:225], v170 offset:55296
	ds_read_b128 v[226:229], v170 offset:56320
	s_mov_b32 m0, s55
	s_nop 0
	global_load_lds_dwordx4 v0, s[14:15]
	s_nop 0
	s_mov_b32 m0, s56
	s_nop 0
	global_load_lds_dwordx4 v147, s[14:15]
	s_add_u32 s12, s16, 0x20080
	s_addc_u32 s13, s17, 0
	s_mov_b32 m0, s59
	s_nop 0
	global_load_lds_dwordx4 v0, s[12:13]
	s_nop 0
	s_mov_b32 m0, s64
	s_nop 0
	global_load_lds_dwordx4 v147, s[12:13]
	s_mov_b32 m0, s57
	s_nop 0
	global_load_lds_dwordx4 v179, s[10:11]
	s_nop 0
	s_mov_b32 m0, s58
	s_nop 0
	global_load_lds_dwordx4 v180, s[10:11]
	s_waitcnt vmcnt(8)
	s_waitcnt lgkmcnt(0)
	s_barrier
	s_setprio 1
	s_waitcnt lgkmcnt(6)
	v_mfma_f32_16x16x128_f8f6f4 v[94:97], v[2:9], v[198:205], v[94:97]
	v_mfma_f32_16x16x128_f8f6f4 v[90:93], v[10:17], v[198:205], v[90:93]
	s_waitcnt lgkmcnt(4)
	v_mfma_f32_16x16x128_f8f6f4 v[78:81], v[2:9], v[206:213], v[78:81]
	v_mfma_f32_16x16x128_f8f6f4 v[74:77], v[10:17], v[206:213], v[74:77]
	s_waitcnt lgkmcnt(2)
	v_mfma_f32_16x16x128_f8f6f4 v[62:65], v[2:9], v[214:221], v[62:65]
	v_mfma_f32_16x16x128_f8f6f4 v[58:61], v[10:17], v[214:221], v[58:61]
	s_waitcnt lgkmcnt(0)
	v_mfma_f32_16x16x128_f8f6f4 v[46:49], v[2:9], v[222:229], v[46:49]
	v_mfma_f32_16x16x128_f8f6f4 v[42:45], v[10:17], v[222:229], v[42:45]
	s_setprio 0
	s_setprio 1
	v_mfma_f32_16x16x128_f8f6f4 v[86:89], v[18:25], v[198:205], v[86:89]
	v_mfma_f32_16x16x128_f8f6f4 v[82:85], v[26:33], v[198:205], v[82:85]
	v_mfma_f32_16x16x128_f8f6f4 v[70:73], v[18:25], v[206:213], v[70:73]
	v_mfma_f32_16x16x128_f8f6f4 v[66:69], v[26:33], v[206:213], v[66:69]
	v_mfma_f32_16x16x128_f8f6f4 v[54:57], v[18:25], v[214:221], v[54:57]
	v_mfma_f32_16x16x128_f8f6f4 v[50:53], v[26:33], v[214:221], v[50:53]
	v_mfma_f32_16x16x128_f8f6f4 v[38:41], v[18:25], v[222:229], v[38:41]
	v_mfma_f32_16x16x128_f8f6f4 v[34:37], v[26:33], v[222:229], v[34:37]
	s_setprio 0
	s_barrier
	s_add_i32 s89, s89, 2
	s_add_u32 s0, s0, 0x100
	s_addc_u32 s1, s1, 0
	s_cmp_gt_u32 s89, 5
	s_mov_b64 s[14:15], s[60:61]
	s_cbranch_scc0 .LBB0_1139
	s_nop 15
	s_nop 15
	s_and_b64 vcc, exec, s[86:87]
	s_cbranch_vccz .LBB0_1142
	s_barrier
.LBB0_1142:
	v_mov_b32_e32 v19, v166
	v_mov_b32_e32 v2, v167
	s_add_i32 s1, s95, 0
	v_lshlrev_b32_e32 v18, 3, v2
	s_add_i32 s1, s1, 0x22200
	v_add_u32_e32 v2, s54, v18
	v_add_u32_e32 v20, s18, v19
	v_lshl_add_u32 v2, v2, 2, s1
	v_lshl_add_u32 v21, v20, 2, s1
	ds_read_b128 v[14:17], v2
	ds_read_b128 v[10:13], v2 offset:16
	ds_read_b128 v[6:9], v2 offset:512
	ds_read_b128 v[2:5], v2 offset:528
	ds_read_b32 v21, v21 offset:2048
	s_waitcnt lgkmcnt(4)
	v_pk_fma_f32 v[28:29], v[160:161], s[100:101], v[14:15]
	s_waitcnt lgkmcnt(3)
	v_pk_fma_f32 v[32:33], v[156:157], s[100:101], v[10:11]
	v_mov_b32_e32 v156, v1
	v_mov_b32_e32 v157, v1
	s_waitcnt lgkmcnt(0)
	v_mul_f32_e32 v24, 0x41800000, v21
	v_pk_mul_f32 v[28:29], v[28:29], v[24:25] op_sel_hi:[1,0]
	v_pk_mul_f32 v[32:33], v[32:33], v[24:25] op_sel_hi:[1,0]
	v_cvt_pk_fp8_f32 v156, v28, v29
	v_cvt_pk_fp8_f32 v157, v32, v33
	v_pk_fma_f32 v[26:27], v[162:163], s[100:101], v[16:17]
	v_pk_fma_f32 v[30:31], v[158:159], s[100:101], v[12:13]
	v_pk_mul_f32 v[26:27], v[26:27], v[24:25] op_sel_hi:[1,0]
	v_pk_mul_f32 v[30:31], v[30:31], v[24:25] op_sel_hi:[1,0]
	v_cvt_pk_fp8_f32 v156, v26, v27 op_sel:[0,0,1]
	v_cvt_pk_fp8_f32 v157, v30, v31 op_sel:[0,0,1]
	v_pk_fma_f32 v[26:27], v[154:155], s[100:101], v[8:9]
	v_pk_fma_f32 v[28:29], v[152:153], s[100:101], v[6:7]
	v_pk_fma_f32 v[30:31], v[150:151], s[100:101], v[4:5]
	v_pk_fma_f32 v[32:33], v[148:149], s[100:101], v[2:3]
	v_pk_mul_f32 v[26:27], v[26:27], v[24:25] op_sel_hi:[1,0]
	v_pk_mul_f32 v[28:29], v[28:29], v[24:25] op_sel_hi:[1,0]
	v_pk_mul_f32 v[30:31], v[30:31], v[24:25] op_sel_hi:[1,0]
	v_pk_mul_f32 v[24:25], v[32:33], v[24:25] op_sel_hi:[1,0]
	v_mov_b32_e32 v32, v1
	v_mov_b32_e32 v33, v1
	s_lshl_b32 s0, s26, 8
	v_cvt_pk_fp8_f32 v32, v28, v29
	v_cvt_pk_fp8_f32 v33, v24, v25
	s_or_b32 s0, s0, s54
	v_add_u32_e32 v18, s0, v18
	s_lshl_b32 s0, s94, 8
	v_add_u32_e32 v22, s0, v20
	v_ashrrev_i32_e32 v23, 31, v22
	v_cvt_pk_fp8_f32 v32, v26, v27 op_sel:[0,0,1]
	v_cvt_pk_fp8_f32 v33, v30, v31 op_sel:[0,0,1]
	v_lshlrev_b64 v[22:23], 10, v[22:23]
	v_ashrrev_i32_e32 v19, 31, v18
	v_lshl_add_u64 v[22:23], s[80:81], 0, v[22:23]
	v_lshl_add_u64 v[22:23], v[22:23], 0, v[18:19]
	v_add_u32_e32 v21, 16, v20
	global_store_dwordx2 v[22:23], v[156:157], off
	global_store_dwordx2 v[22:23], v[32:33], off offset:128
	v_lshl_add_u32 v22, v21, 2, s1
	ds_read_b32 v24, v22 offset:2048
	v_pk_fma_f32 v[28:29], v[142:143], s[100:101], v[14:15]
	v_pk_fma_f32 v[32:33], v[138:139], s[100:101], v[10:11]
	v_mov_b32_e32 v138, v1
	v_mov_b32_e32 v139, v1
	s_waitcnt lgkmcnt(0)
; #define LAS __attribute__((address_space(3)))
; __device__ __forceinline__ unsigned cvt_fp8x4(float a, float b, float c, float d) { int w = __builtin_amdgcn_cvt_pk_fp8_f32(a, b, 0, false); w = __builtin_amdgcn_cvt_pk_fp8_f32(c, d, w, true); return (unsigned)w; }
;     __device__ __forceinline__ void operator()(const f32x4 (&acc)[2][2][4][2], const Unit& u, int wr, int wc, int fr, int fq, const LAS unsigned char* epl) const {
;     ...
;         for (int ai = 0; ai < 2; ++ai)
; #pragma unroll
;             for (int m = 0; m < 4; ++m) { const int sl = ai * HALF + wr * 64 + m * 16 + fr;
;                 const float gate = *(const LAS float*)(epl + 2048 + sl * 4);
;                 unsigned char* rowp = (unsigned char*)YK + (size_t)(u.pm * BM + sl) * DM + col0;
;                 const float g8 = gate * YK8_SCALE;
; #pragma unroll
;                 for (int bj = 0; bj < 2; ++bj) { const f32x4 a0 = (acc[ai][bj][m][0] + bv[bj][0]) * g8, a1 = (acc[ai][bj][m][1] + bv[bj][1]) * g8;
;                     u32x2 w8; w8.x = cvt_fp8x4(a0[0], a0[1], a0[2], a0[3]); w8.y = cvt_fp8x4(a1[0], a1[1], a1[2], a1[3]); *(u32x2*)(rowp + bj * HALF) = w8; } }
	v_mul_f32_e32 v24, 0x41800000, v24
	v_pk_mul_f32 v[28:29], v[28:29], v[24:25] op_sel_hi:[1,0]
	v_pk_mul_f32 v[32:33], v[32:33], v[24:25] op_sel_hi:[1,0]
	v_cvt_pk_fp8_f32 v138, v28, v29
	v_cvt_pk_fp8_f32 v139, v32, v33
	v_pk_fma_f32 v[26:27], v[144:145], s[100:101], v[16:17]
	v_pk_fma_f32 v[30:31], v[140:141], s[100:101], v[12:13]
	v_pk_mul_f32 v[26:27], v[26:27], v[24:25] op_sel_hi:[1,0]
	v_pk_mul_f32 v[30:31], v[30:31], v[24:25] op_sel_hi:[1,0]
	v_cvt_pk_fp8_f32 v138, v26, v27 op_sel:[0,0,1]
	v_cvt_pk_fp8_f32 v139, v30, v31 op_sel:[0,0,1]
	v_pk_fma_f32 v[26:27], v[136:137], s[100:101], v[8:9]
	v_pk_fma_f32 v[28:29], v[134:135], s[100:101], v[6:7]
	v_pk_fma_f32 v[30:31], v[132:133], s[100:101], v[4:5]
	v_pk_fma_f32 v[32:33], v[130:131], s[100:101], v[2:3]
	v_pk_mul_f32 v[26:27], v[26:27], v[24:25] op_sel_hi:[1,0]
	v_pk_mul_f32 v[28:29], v[28:29], v[24:25] op_sel_hi:[1,0]
	v_pk_mul_f32 v[30:31], v[30:31], v[24:25] op_sel_hi:[1,0]
	v_pk_mul_f32 v[24:25], v[32:33], v[24:25] op_sel_hi:[1,0]
	v_mov_b32_e32 v32, v1
	v_mov_b32_e32 v33, v1
	v_cvt_pk_fp8_f32 v32, v28, v29
	v_cvt_pk_fp8_f32 v33, v24, v25
	v_add_u32_e32 v22, s0, v21
	v_ashrrev_i32_e32 v23, 31, v22
	v_cvt_pk_fp8_f32 v32, v26, v27 op_sel:[0,0,1]
	v_cvt_pk_fp8_f32 v33, v30, v31 op_sel:[0,0,1]
	v_lshlrev_b64 v[22:23], 10, v[22:23]
	v_lshl_add_u64 v[22:23], s[80:81], 0, v[22:23]
	v_lshl_add_u64 v[22:23], v[22:23], 0, v[18:19]
	v_add_u32_e32 v21, 32, v20
	global_store_dwordx2 v[22:23], v[138:139], off
	global_store_dwordx2 v[22:23], v[32:33], off offset:128
	v_lshl_add_u32 v22, v21, 2, s1
	ds_read_b32 v24, v22 offset:2048
	v_pk_fma_f32 v[28:29], v[126:127], s[100:101], v[14:15]
	v_pk_fma_f32 v[32:33], v[122:123], s[100:101], v[10:11]
	v_mov_b32_e32 v122, v1
	v_mov_b32_e32 v123, v1
	s_waitcnt lgkmcnt(0)
	v_mul_f32_e32 v24, 0x41800000, v24
	v_pk_mul_f32 v[28:29], v[28:29], v[24:25] op_sel_hi:[1,0]
	v_pk_mul_f32 v[32:33], v[32:33], v[24:25] op_sel_hi:[1,0]
	v_cvt_pk_fp8_f32 v122, v28, v29
	v_cvt_pk_fp8_f32 v123, v32, v33
	v_pk_fma_f32 v[26:27], v[128:129], s[100:101], v[16:17]
	v_pk_fma_f32 v[30:31], v[124:125], s[100:101], v[12:13]
	v_pk_mul_f32 v[26:27], v[26:27], v[24:25] op_sel_hi:[1,0]
	v_pk_mul_f32 v[30:31], v[30:31], v[24:25] op_sel_hi:[1,0]
	v_cvt_pk_fp8_f32 v122, v26, v27 op_sel:[0,0,1]
	v_cvt_pk_fp8_f32 v123, v30, v31 op_sel:[0,0,1]
	v_pk_fma_f32 v[26:27], v[120:121], s[100:101], v[8:9]
	v_pk_fma_f32 v[28:29], v[118:119], s[100:101], v[6:7]
	v_pk_fma_f32 v[30:31], v[116:117], s[100:101], v[4:5]
	v_pk_fma_f32 v[32:33], v[114:115], s[100:101], v[2:3]
	v_pk_mul_f32 v[26:27], v[26:27], v[24:25] op_sel_hi:[1,0]
	v_pk_mul_f32 v[28:29], v[28:29], v[24:25] op_sel_hi:[1,0]
	v_pk_mul_f32 v[30:31], v[30:31], v[24:25] op_sel_hi:[1,0]
	v_pk_mul_f32 v[24:25], v[32:33], v[24:25] op_sel_hi:[1,0]
	v_mov_b32_e32 v32, v1
	v_mov_b32_e32 v33, v1
	v_cvt_pk_fp8_f32 v32, v28, v29
	v_cvt_pk_fp8_f32 v33, v24, v25
	v_add_u32_e32 v22, s0, v21
	v_ashrrev_i32_e32 v23, 31, v22
	v_cvt_pk_fp8_f32 v32, v26, v27 op_sel:[0,0,1]
	v_cvt_pk_fp8_f32 v33, v30, v31 op_sel:[0,0,1]
	v_lshlrev_b64 v[22:23], 10, v[22:23]
	v_lshl_add_u64 v[22:23], s[80:81], 0, v[22:23]
	v_lshl_add_u64 v[22:23], v[22:23], 0, v[18:19]
	v_add_u32_e32 v21, 48, v20
	global_store_dwordx2 v[22:23], v[122:123], off
	global_store_dwordx2 v[22:23], v[32:33], off offset:128
	v_lshl_add_u32 v22, v21, 2, s1
	ds_read_b32 v24, v22 offset:2048
	v_pk_fma_f32 v[28:29], v[110:111], s[100:101], v[14:15]
	v_pk_fma_f32 v[32:33], v[106:107], s[100:101], v[10:11]
	v_mov_b32_e32 v106, v1
	v_mov_b32_e32 v107, v1
	s_waitcnt lgkmcnt(0)
	v_mul_f32_e32 v24, 0x41800000, v24
	v_pk_mul_f32 v[28:29], v[28:29], v[24:25] op_sel_hi:[1,0]
	v_pk_mul_f32 v[32:33], v[32:33], v[24:25] op_sel_hi:[1,0]
	v_cvt_pk_fp8_f32 v106, v28, v29
	v_cvt_pk_fp8_f32 v107, v32, v33
	v_pk_fma_f32 v[26:27], v[112:113], s[100:101], v[16:17]
	v_pk_fma_f32 v[30:31], v[108:109], s[100:101], v[12:13]
	v_pk_mul_f32 v[26:27], v[26:27], v[24:25] op_sel_hi:[1,0]
	v_pk_mul_f32 v[30:31], v[30:31], v[24:25] op_sel_hi:[1,0]
	v_cvt_pk_fp8_f32 v106, v26, v27 op_sel:[0,0,1]
	v_cvt_pk_fp8_f32 v107, v30, v31 op_sel:[0,0,1]
	v_pk_fma_f32 v[26:27], v[104:105], s[100:101], v[8:9]
	v_pk_fma_f32 v[28:29], v[102:103], s[100:101], v[6:7]
	v_pk_fma_f32 v[30:31], v[100:101], s[100:101], v[4:5]
	v_pk_fma_f32 v[32:33], v[98:99], s[100:101], v[2:3]
	v_pk_mul_f32 v[26:27], v[26:27], v[24:25] op_sel_hi:[1,0]
	v_pk_mul_f32 v[28:29], v[28:29], v[24:25] op_sel_hi:[1,0]
	v_pk_mul_f32 v[30:31], v[30:31], v[24:25] op_sel_hi:[1,0]
	v_pk_mul_f32 v[24:25], v[32:33], v[24:25] op_sel_hi:[1,0]
	v_mov_b32_e32 v32, v1
	v_mov_b32_e32 v33, v1
	v_cvt_pk_fp8_f32 v32, v28, v29
	v_cvt_pk_fp8_f32 v33, v24, v25
	v_add_u32_e32 v22, s0, v21
	v_ashrrev_i32_e32 v23, 31, v22
	v_cvt_pk_fp8_f32 v32, v26, v27 op_sel:[0,0,1]
	v_cvt_pk_fp8_f32 v33, v30, v31 op_sel:[0,0,1]
	v_lshlrev_b64 v[22:23], 10, v[22:23]
	v_lshl_add_u64 v[22:23], s[80:81], 0, v[22:23]
	v_lshl_add_u64 v[22:23], v[22:23], 0, v[18:19]
	v_add_u32_e32 v21, 0x80, v20
	global_store_dwordx2 v[22:23], v[106:107], off
	global_store_dwordx2 v[22:23], v[32:33], off offset:128
	v_lshl_add_u32 v22, v21, 2, s1
	ds_read_b32 v24, v22 offset:2048
	v_pk_fma_f32 v[28:29], v[94:95], s[100:101], v[14:15]
	v_pk_fma_f32 v[32:33], v[90:91], s[100:101], v[10:11]
	v_mov_b32_e32 v90, v1
	v_mov_b32_e32 v91, v1
	s_waitcnt lgkmcnt(0)
; #define LAS __attribute__((address_space(3)))
; __device__ __forceinline__ unsigned cvt_fp8x4(float a, float b, float c, float d) { int w = __builtin_amdgcn_cvt_pk_fp8_f32(a, b, 0, false); w = __builtin_amdgcn_cvt_pk_fp8_f32(c, d, w, true); return (unsigned)w; }
;     __device__ __forceinline__ void operator()(const f32x4 (&acc)[2][2][4][2], const Unit& u, int wr, int wc, int fr, int fq, const LAS unsigned char* epl) const {
;     ...
;         for (int ai = 0; ai < 2; ++ai)
; #pragma unroll
;             for (int m = 0; m < 4; ++m) { const int sl = ai * HALF + wr * 64 + m * 16 + fr;
;                 const float gate = *(const LAS float*)(epl + 2048 + sl * 4);
;                 unsigned char* rowp = (unsigned char*)YK + (size_t)(u.pm * BM + sl) * DM + col0;
;                 const float g8 = gate * YK8_SCALE;
; #pragma unroll
;                 for (int bj = 0; bj < 2; ++bj) { const f32x4 a0 = (acc[ai][bj][m][0] + bv[bj][0]) * g8, a1 = (acc[ai][bj][m][1] + bv[bj][1]) * g8;
;                     u32x2 w8; w8.x = cvt_fp8x4(a0[0], a0[1], a0[2], a0[3]); w8.y = cvt_fp8x4(a1[0], a1[1], a1[2], a1[3]); *(u32x2*)(rowp + bj * HALF) = w8; } }
	v_mul_f32_e32 v24, 0x41800000, v24
	v_pk_mul_f32 v[28:29], v[28:29], v[24:25] op_sel_hi:[1,0]
	v_pk_mul_f32 v[32:33], v[32:33], v[24:25] op_sel_hi:[1,0]
	v_cvt_pk_fp8_f32 v90, v28, v29
	v_cvt_pk_fp8_f32 v91, v32, v33
	v_pk_fma_f32 v[26:27], v[96:97], s[100:101], v[16:17]
	v_pk_fma_f32 v[30:31], v[92:93], s[100:101], v[12:13]
	v_pk_mul_f32 v[26:27], v[26:27], v[24:25] op_sel_hi:[1,0]
	v_pk_mul_f32 v[30:31], v[30:31], v[24:25] op_sel_hi:[1,0]
	v_cvt_pk_fp8_f32 v90, v26, v27 op_sel:[0,0,1]
	v_cvt_pk_fp8_f32 v91, v30, v31 op_sel:[0,0,1]
	v_pk_fma_f32 v[26:27], v[88:89], s[100:101], v[8:9]
	v_pk_fma_f32 v[28:29], v[86:87], s[100:101], v[6:7]
	v_pk_fma_f32 v[30:31], v[84:85], s[100:101], v[4:5]
	v_pk_fma_f32 v[32:33], v[82:83], s[100:101], v[2:3]
	v_pk_mul_f32 v[26:27], v[26:27], v[24:25] op_sel_hi:[1,0]
	v_pk_mul_f32 v[28:29], v[28:29], v[24:25] op_sel_hi:[1,0]
	v_pk_mul_f32 v[30:31], v[30:31], v[24:25] op_sel_hi:[1,0]
	v_pk_mul_f32 v[24:25], v[32:33], v[24:25] op_sel_hi:[1,0]
	v_mov_b32_e32 v32, v1
	v_mov_b32_e32 v33, v1
	v_cvt_pk_fp8_f32 v32, v28, v29
	v_cvt_pk_fp8_f32 v33, v24, v25
	v_add_u32_e32 v22, s0, v21
	v_ashrrev_i32_e32 v23, 31, v22
	v_cvt_pk_fp8_f32 v32, v26, v27 op_sel:[0,0,1]
	v_cvt_pk_fp8_f32 v33, v30, v31 op_sel:[0,0,1]
	v_lshlrev_b64 v[22:23], 10, v[22:23]
	v_lshl_add_u64 v[22:23], s[80:81], 0, v[22:23]
	v_lshl_add_u64 v[22:23], v[22:23], 0, v[18:19]
	v_add_u32_e32 v21, 0x90, v20
	global_store_dwordx2 v[22:23], v[90:91], off
	global_store_dwordx2 v[22:23], v[32:33], off offset:128
	v_lshl_add_u32 v22, v21, 2, s1
	ds_read_b32 v24, v22 offset:2048
	v_pk_fma_f32 v[28:29], v[78:79], s[100:101], v[14:15]
	v_pk_fma_f32 v[32:33], v[74:75], s[100:101], v[10:11]
	v_mov_b32_e32 v74, v1
	v_mov_b32_e32 v75, v1
	s_waitcnt lgkmcnt(0)
	v_mul_f32_e32 v24, 0x41800000, v24
	v_pk_mul_f32 v[28:29], v[28:29], v[24:25] op_sel_hi:[1,0]
	v_pk_mul_f32 v[32:33], v[32:33], v[24:25] op_sel_hi:[1,0]
	v_cvt_pk_fp8_f32 v74, v28, v29
	v_cvt_pk_fp8_f32 v75, v32, v33
	v_pk_fma_f32 v[26:27], v[80:81], s[100:101], v[16:17]
	v_pk_fma_f32 v[30:31], v[76:77], s[100:101], v[12:13]
	v_pk_mul_f32 v[26:27], v[26:27], v[24:25] op_sel_hi:[1,0]
	v_pk_mul_f32 v[30:31], v[30:31], v[24:25] op_sel_hi:[1,0]
	v_cvt_pk_fp8_f32 v74, v26, v27 op_sel:[0,0,1]
	v_cvt_pk_fp8_f32 v75, v30, v31 op_sel:[0,0,1]
	v_pk_fma_f32 v[26:27], v[72:73], s[100:101], v[8:9]
	v_pk_fma_f32 v[28:29], v[70:71], s[100:101], v[6:7]
	v_pk_fma_f32 v[30:31], v[68:69], s[100:101], v[4:5]
	v_pk_fma_f32 v[32:33], v[66:67], s[100:101], v[2:3]
	v_pk_mul_f32 v[26:27], v[26:27], v[24:25] op_sel_hi:[1,0]
	v_pk_mul_f32 v[28:29], v[28:29], v[24:25] op_sel_hi:[1,0]
	v_pk_mul_f32 v[30:31], v[30:31], v[24:25] op_sel_hi:[1,0]
	v_pk_mul_f32 v[24:25], v[32:33], v[24:25] op_sel_hi:[1,0]
	v_mov_b32_e32 v32, v1
	v_mov_b32_e32 v33, v1
	v_cvt_pk_fp8_f32 v32, v28, v29
	v_cvt_pk_fp8_f32 v33, v24, v25
	v_add_u32_e32 v22, s0, v21
	v_ashrrev_i32_e32 v23, 31, v22
	v_cvt_pk_fp8_f32 v32, v26, v27 op_sel:[0,0,1]
	v_cvt_pk_fp8_f32 v33, v30, v31 op_sel:[0,0,1]
	v_lshlrev_b64 v[22:23], 10, v[22:23]
	v_lshl_add_u64 v[22:23], s[80:81], 0, v[22:23]
	v_lshl_add_u64 v[22:23], v[22:23], 0, v[18:19]
	v_add_u32_e32 v21, 0xa0, v20
	global_store_dwordx2 v[22:23], v[74:75], off
	global_store_dwordx2 v[22:23], v[32:33], off offset:128
	v_lshl_add_u32 v22, v21, 2, s1
	ds_read_b32 v24, v22 offset:2048
	v_pk_fma_f32 v[28:29], v[62:63], s[100:101], v[14:15]
	v_pk_fma_f32 v[32:33], v[58:59], s[100:101], v[10:11]
	v_mov_b32_e32 v58, v1
	v_mov_b32_e32 v59, v1
	s_waitcnt lgkmcnt(0)
	v_mul_f32_e32 v24, 0x41800000, v24
	v_pk_mul_f32 v[28:29], v[28:29], v[24:25] op_sel_hi:[1,0]
	v_pk_mul_f32 v[32:33], v[32:33], v[24:25] op_sel_hi:[1,0]
	v_cvt_pk_fp8_f32 v58, v28, v29
	v_cvt_pk_fp8_f32 v59, v32, v33
	v_pk_fma_f32 v[26:27], v[64:65], s[100:101], v[16:17]
	v_pk_fma_f32 v[30:31], v[60:61], s[100:101], v[12:13]
	v_pk_mul_f32 v[26:27], v[26:27], v[24:25] op_sel_hi:[1,0]
	v_pk_mul_f32 v[30:31], v[30:31], v[24:25] op_sel_hi:[1,0]
	v_cvt_pk_fp8_f32 v58, v26, v27 op_sel:[0,0,1]
	v_cvt_pk_fp8_f32 v59, v30, v31 op_sel:[0,0,1]
	v_pk_fma_f32 v[26:27], v[56:57], s[100:101], v[8:9]
	v_pk_fma_f32 v[28:29], v[54:55], s[100:101], v[6:7]
	v_pk_fma_f32 v[30:31], v[52:53], s[100:101], v[4:5]
	v_pk_fma_f32 v[32:33], v[50:51], s[100:101], v[2:3]
	v_pk_mul_f32 v[26:27], v[26:27], v[24:25] op_sel_hi:[1,0]
	v_pk_mul_f32 v[28:29], v[28:29], v[24:25] op_sel_hi:[1,0]
	v_pk_mul_f32 v[30:31], v[30:31], v[24:25] op_sel_hi:[1,0]
	v_pk_mul_f32 v[24:25], v[32:33], v[24:25] op_sel_hi:[1,0]
	v_mov_b32_e32 v32, v1
	v_mov_b32_e32 v33, v1
	v_cvt_pk_fp8_f32 v32, v28, v29
	v_cvt_pk_fp8_f32 v33, v24, v25
	v_add_u32_e32 v22, s0, v21
	v_ashrrev_i32_e32 v23, 31, v22
	v_cvt_pk_fp8_f32 v32, v26, v27 op_sel:[0,0,1]
	v_cvt_pk_fp8_f32 v33, v30, v31 op_sel:[0,0,1]
	v_add_u32_e32 v20, 0xb0, v20
	v_lshlrev_b64 v[22:23], 10, v[22:23]
	v_lshl_add_u32 v21, v20, 2, s1
	v_lshl_add_u64 v[22:23], s[80:81], 0, v[22:23]
	ds_read_b32 v21, v21 offset:2048
	v_lshl_add_u64 v[22:23], v[22:23], 0, v[18:19]
	global_store_dwordx2 v[22:23], v[58:59], off
	global_store_dwordx2 v[22:23], v[32:33], off offset:128
	v_add_u32_e32 v22, s0, v20
	v_ashrrev_i32_e32 v23, 31, v22
	v_lshlrev_b64 v[22:23], 10, v[22:23]
	v_lshl_add_u64 v[22:23], s[80:81], 0, v[22:23]
	s_waitcnt lgkmcnt(0)
	v_mul_f32_e32 v20, 0x41800000, v21
	v_pk_fma_f32 v[10:11], v[42:43], s[100:101], v[10:11]
	v_lshl_add_u64 v[18:19], v[22:23], 0, v[18:19]
	v_pk_fma_f32 v[14:15], v[46:47], s[100:101], v[14:15]
	v_pk_mul_f32 v[10:11], v[10:11], v[20:21] op_sel_hi:[1,0]
	v_mov_b32_e32 v23, v1
	v_pk_fma_f32 v[6:7], v[38:39], s[100:101], v[6:7]
	v_pk_fma_f32 v[2:3], v[34:35], s[100:101], v[2:3]
	v_pk_mul_f32 v[14:15], v[14:15], v[20:21] op_sel_hi:[1,0]
	v_mov_b32_e32 v22, v1
	v_cvt_pk_fp8_f32 v23, v10, v11
	v_pk_mul_f32 v[6:7], v[6:7], v[20:21] op_sel_hi:[1,0]
	v_pk_mul_f32 v[2:3], v[2:3], v[20:21] op_sel_hi:[1,0]
	v_mov_b32_e32 v10, v1
	v_mov_b32_e32 v11, v1
	v_cvt_pk_fp8_f32 v22, v14, v15
	v_cvt_pk_fp8_f32 v10, v6, v7
	v_cvt_pk_fp8_f32 v11, v2, v3
	v_pk_fma_f32 v[16:17], v[48:49], s[100:101], v[16:17]
	v_pk_fma_f32 v[12:13], v[44:45], s[100:101], v[12:13]
	v_pk_fma_f32 v[8:9], v[40:41], s[100:101], v[8:9]
	v_pk_fma_f32 v[4:5], v[36:37], s[100:101], v[4:5]
	v_pk_mul_f32 v[16:17], v[16:17], v[20:21] op_sel_hi:[1,0]
	v_pk_mul_f32 v[12:13], v[12:13], v[20:21] op_sel_hi:[1,0]
	v_pk_mul_f32 v[8:9], v[8:9], v[20:21] op_sel_hi:[1,0]
	v_pk_mul_f32 v[4:5], v[4:5], v[20:21] op_sel_hi:[1,0]
	v_cvt_pk_fp8_f32 v22, v16, v17 op_sel:[0,0,1]
	v_cvt_pk_fp8_f32 v23, v12, v13 op_sel:[0,0,1]
	v_cvt_pk_fp8_f32 v10, v8, v9 op_sel:[0,0,1]
	v_cvt_pk_fp8_f32 v11, v4, v5 op_sel:[0,0,1]
	s_mov_b64 s[0:1], -1
	s_and_b64 vcc, exec, s[2:3]
	global_store_dwordx2 v[18:19], v[22:23], off
	global_store_dwordx2 v[18:19], v[10:11], off offset:128
	s_cbranch_vccnz .LBB0_1122
	s_andn2_b64 vcc, exec, s[78:79]
	s_cbranch_vccnz .LBB0_1121
	s_barrier
	s_branch .LBB0_1121
